# top-k gather: expert input panel stores non-temporal
# baseline (speedup 1.0000x reference)
.LBB0_1356:
	ds_read_b128 v[4:7], v86
	ds_read_b128 v[10:13], v86 offset:16
	ds_read_b128 v[20:23], v86 offset:32
	ds_read_b128 v[28:31], v86 offset:48
	ds_read_b128 v[36:39], v86 offset:64
	ds_read_b128 v[44:47], v86 offset:80
	s_waitcnt lgkmcnt(4)
	v_xad_u32 v10, v10, -1, s34
	s_waitcnt lgkmcnt(3)
	v_xad_u32 v18, v20, -1, s34
	v_ashrrev_i32_e32 v11, 31, v10
	v_ashrrev_i32_e32 v19, 31, v18
	v_xad_u32 v2, v4, -1, s34
	v_lshlrev_b64 v[10:11], 10, v[10:11]
	v_lshlrev_b64 v[18:19], 10, v[18:19]
	v_ashrrev_i32_e32 v3, 31, v2
	v_xad_u32 v6, v6, -1, s34
	v_lshl_add_u64 v[10:11], v[64:65], 0, v[10:11]
	v_lshl_add_u64 v[18:19], v[64:65], 0, v[18:19]
	v_lshlrev_b64 v[2:3], 10, v[2:3]
	v_ashrrev_i32_e32 v7, 31, v6
	global_load_dwordx4 v[14:17], v[10:11], off
	v_lshl_add_u64 v[2:3], v[64:65], 0, v[2:3]
	global_load_dwordx4 v[18:21], v[18:19], off
	v_xad_u32 v10, v12, -1, s34
	v_lshlrev_b64 v[6:7], 10, v[6:7]
	v_ashrrev_i32_e32 v11, 31, v10
	global_load_dwordx4 v[2:5], v[2:3], off
	v_lshl_add_u64 v[6:7], v[64:65], 0, v[6:7]
	v_lshlrev_b64 v[10:11], 10, v[10:11]
	v_xad_u32 v22, v22, -1, s34
	ds_read_b128 v[52:55], v86 offset:96
	ds_read_b128 v[88:91], v86 offset:112
	global_load_dwordx4 v[6:9], v[6:7], off
	v_lshl_add_u64 v[10:11], v[64:65], 0, v[10:11]
	v_ashrrev_i32_e32 v23, 31, v22
	s_waitcnt lgkmcnt(4)
	v_xad_u32 v26, v28, -1, s34
	s_waitcnt lgkmcnt(3)
	v_xad_u32 v34, v36, -1, s34
	global_load_dwordx4 v[10:13], v[10:11], off
	v_lshlrev_b64 v[22:23], 10, v[22:23]
	v_ashrrev_i32_e32 v27, 31, v26
	v_xad_u32 v30, v30, -1, s34
	v_ashrrev_i32_e32 v35, 31, v34
	v_xad_u32 v38, v38, -1, s34
	v_lshl_add_u64 v[22:23], v[64:65], 0, v[22:23]
	v_lshlrev_b64 v[26:27], 10, v[26:27]
	v_ashrrev_i32_e32 v31, 31, v30
	v_lshlrev_b64 v[34:35], 10, v[34:35]
	v_ashrrev_i32_e32 v39, 31, v38
	s_waitcnt lgkmcnt(2)
	v_xad_u32 v42, v44, -1, s34
	global_load_dwordx4 v[22:25], v[22:23], off
	v_lshl_add_u64 v[26:27], v[64:65], 0, v[26:27]
	v_lshlrev_b64 v[30:31], 10, v[30:31]
	v_lshl_add_u64 v[34:35], v[64:65], 0, v[34:35]
	v_lshlrev_b64 v[38:39], 10, v[38:39]
	v_ashrrev_i32_e32 v43, 31, v42
	v_xad_u32 v46, v46, -1, s34
	global_load_dwordx4 v[26:29], v[26:27], off
	v_lshl_add_u64 v[30:31], v[64:65], 0, v[30:31]
	global_load_dwordx4 v[34:37], v[34:35], off
	v_lshl_add_u64 v[38:39], v[64:65], 0, v[38:39]
	v_lshlrev_b64 v[42:43], 10, v[42:43]
	v_ashrrev_i32_e32 v47, 31, v46
	s_waitcnt lgkmcnt(1)
	v_xad_u32 v50, v52, -1, s34
	global_load_dwordx4 v[30:33], v[30:31], off
	v_lshl_add_u64 v[42:43], v[64:65], 0, v[42:43]
	global_load_dwordx4 v[38:41], v[38:39], off
	v_lshlrev_b64 v[46:47], 10, v[46:47]
	v_ashrrev_i32_e32 v51, 31, v50
	v_xad_u32 v54, v54, -1, s34
	global_load_dwordx4 v[42:45], v[42:43], off
	v_lshl_add_u64 v[46:47], v[64:65], 0, v[46:47]
	v_lshlrev_b64 v[50:51], 10, v[50:51]
	v_ashrrev_i32_e32 v55, 31, v54
	s_waitcnt lgkmcnt(0)
	v_xad_u32 v58, v88, -1, s34
	global_load_dwordx4 v[46:49], v[46:47], off
	v_lshl_add_u64 v[50:51], v[64:65], 0, v[50:51]
	v_lshlrev_b64 v[54:55], 10, v[54:55]
	v_ashrrev_i32_e32 v59, 31, v58
	v_xad_u32 v88, v90, -1, s34
	global_load_dwordx4 v[50:53], v[50:51], off
	v_lshl_add_u64 v[54:55], v[64:65], 0, v[54:55]
	v_lshlrev_b64 v[58:59], 10, v[58:59]
	v_ashrrev_i32_e32 v89, 31, v88
	global_load_dwordx4 v[54:57], v[54:55], off
	v_lshl_add_u64 v[58:59], v[64:65], 0, v[58:59]
	v_lshlrev_b64 v[88:89], 10, v[88:89]
	global_load_dwordx4 v[58:61], v[58:59], off
	v_lshl_add_u64 v[88:89], v[64:65], 0, v[88:89]
	global_load_dwordx4 v[88:91], v[88:89], off
	s_movk_i32 s10, 0xd000
	v_add_co_u32_e32 v92, vcc, s10, v76
	s_movk_i32 s10, 0xe000
	s_nop 0
	v_addc_co_u32_e32 v93, vcc, -1, v77, vcc
	s_waitcnt vmcnt(13)
	global_store_dwordx4 v[92:93], v[2:5], off offset:-3072 nt
	s_waitcnt vmcnt(13)
	global_store_dwordx4 v[92:93], v[6:9], off offset:-2048 nt
	global_store_dwordx4 v[92:93], v[14:17], off offset:-1024 nt
	v_add_co_u32_e32 v2, vcc, s10, v76
	s_movk_i32 s10, 0xf000
	s_nop 0
	v_addc_co_u32_e32 v3, vcc, -1, v77, vcc
	s_waitcnt vmcnt(14)
	global_store_dwordx4 v[2:3], v[10:13], off offset:-4096 nt
	global_store_dwordx4 v[2:3], v[18:21], off offset:-3072 nt
	s_waitcnt vmcnt(15)
	global_store_dwordx4 v[2:3], v[22:25], off offset:-2048 nt
	s_waitcnt vmcnt(15)
	global_store_dwordx4 v[2:3], v[26:29], off offset:-1024 nt
	s_waitcnt vmcnt(14)
	global_store_dwordx4 v[2:3], v[30:33], off nt
	v_add_co_u32_e32 v2, vcc, s10, v76
	v_add_u32_e32 v87, 0x80, v87
	s_nop 0
	v_addc_co_u32_e32 v3, vcc, -1, v77, vcc
	s_mov_b64 s[10:11], 0x20000
	v_cmp_lt_i32_e32 vcc, s55, v87
	global_store_dwordx4 v[2:3], v[34:37], off offset:-3072 nt
	s_waitcnt vmcnt(15)
	global_store_dwordx4 v[2:3], v[38:41], off offset:-2048 nt
	s_waitcnt vmcnt(15)
	global_store_dwordx4 v[2:3], v[42:45], off offset:-1024 nt
	s_waitcnt vmcnt(15)
	global_store_dwordx4 v[76:77], v[46:49], off offset:-4096 nt
	s_waitcnt vmcnt(15)
	global_store_dwordx4 v[76:77], v[50:53], off offset:-3072 nt
	s_waitcnt vmcnt(15)
	global_store_dwordx4 v[76:77], v[54:57], off offset:-2048 nt
	s_waitcnt vmcnt(15)
	global_store_dwordx4 v[76:77], v[58:61], off offset:-1024 nt
	s_waitcnt vmcnt(15)
	global_store_dwordx4 v[76:77], v[88:91], off nt
	v_lshl_add_u64 v[76:77], v[76:77], 0, s[10:11]
	v_add_u32_e32 v86, 0x400, v86
	s_or_b64 s[8:9], vcc, s[8:9]
	s_andn2_b64 exec, exec, s[8:9]
	s_cbranch_execnz .LBB0_1356

.LBB0_1358:
	s_andn2_b64 vcc, exec, s[6:7]
	s_cbranch_vccnz .LBB0_1319
	ds_read_b128 v[2:5], v81
	ds_read_b128 v[6:9], v81 offset:16
	v_lshl_add_u64 v[18:19], s[16:17], 0, v[130:131]
	v_lshl_add_u64 v[18:19], v[18:19], 0, v[62:63]
	v_lshl_add_u64 v[20:21], v[18:19], 0, v[66:67]
	s_waitcnt lgkmcnt(1)
	v_xad_u32 v2, v2, -1, s34
	s_waitcnt lgkmcnt(0)
	v_xad_u32 v6, v6, -1, s34
	v_ashrrev_i32_e32 v3, 31, v2
	v_ashrrev_i32_e32 v7, 31, v6
	v_lshlrev_b64 v[2:3], 10, v[2:3]
	v_lshlrev_b64 v[6:7], 10, v[6:7]
	v_lshl_add_u64 v[2:3], v[64:65], 0, v[2:3]
	v_lshl_add_u64 v[6:7], v[64:65], 0, v[6:7]
	global_load_dwordx4 v[10:13], v[2:3], off
	global_load_dwordx4 v[14:17], v[6:7], off
	v_xad_u32 v2, v4, -1, s34
	v_ashrrev_i32_e32 v3, 31, v2
	v_lshlrev_b64 v[2:3], 10, v[2:3]
	v_xad_u32 v6, v8, -1, s34
	v_lshl_add_u64 v[2:3], v[64:65], 0, v[2:3]
	v_ashrrev_i32_e32 v7, 31, v6
	global_load_dwordx4 v[2:5], v[2:3], off
	v_lshlrev_b64 v[6:7], 10, v[6:7]
	v_lshl_add_u64 v[6:7], v[64:65], 0, v[6:7]
	global_load_dwordx4 v[6:9], v[6:7], off
	s_waitcnt vmcnt(3)
	global_store_dwordx4 v[20:21], v[10:13], off nt
	s_nop 1
	v_lshl_add_u64 v[10:11], v[18:19], 0, v[68:69]
	s_waitcnt vmcnt(2)
	global_store_dwordx4 v[10:11], v[2:5], off nt
	s_nop 1
	v_lshl_add_u64 v[2:3], v[18:19], 0, v[70:71]
	global_store_dwordx4 v[2:3], v[14:17], off nt
	v_lshl_add_u64 v[2:3], v[18:19], 0, v[72:73]
	s_waitcnt vmcnt(3)
	global_store_dwordx4 v[2:3], v[6:9], off nt
	s_branch .LBB0_1319
